# loop-edge rotation: output-wave loop back edge is one conditional branch after the barrier (counter bump hoisted before barrier); loader even half falls through into odd half
# baseline (speedup 1.0000x reference)
.Lld_even:
	s_add_i32 s5, s0, -2
	ds_read_b128 v[194:197], v193
	ds_read_b128 v[198:201], v193 offset:32
	ds_read_b128 v[202:205], v193 offset:64
	ds_read_b128 v[206:209], v193 offset:96
	s_waitcnt lgkmcnt(3)
	v_mfma_f32_32x32x16_f16 v[66:81], v[98:101], v[194:197], v[2:17]
	s_waitcnt lgkmcnt(2)
	v_mfma_f32_32x32x16_f16 v[66:81], v[102:105], v[198:201], v[66:81]
	s_waitcnt lgkmcnt(1)
	v_mfma_f32_32x32x16_f16 v[66:81], v[106:109], v[202:205], v[66:81]
	s_waitcnt lgkmcnt(0)
	v_mfma_f32_32x32x16_f16 v[66:81], v[110:113], v[206:209], v[66:81]
	v_mfma_f32_32x32x16_f16 v[82:97], v[114:117], v[194:197], v[18:33]
	s_nop 10
	v_and_b32_e32 v66, 0xffffffc0, v66
	v_and_or_b32 v67, v67, s1, 1
	v_and_or_b32 v68, v68, s1, 2
	v_and_or_b32 v69, v69, s1, 3
	v_med3_f32 v211, v66, v67, s4
	v_and_or_b32 v70, v70, s1, 4
	v_min3_f32 v210, v66, s4, v67
	v_and_or_b32 v71, v71, s1, 5
	v_mfma_f32_32x32x16_f16 v[82:97], v[118:121], v[198:201], v[82:97]
	v_med3_f32 v214, v210, v68, v69
	v_and_or_b32 v72, v72, s1, 6
	v_min3_f32 v212, v210, v68, v69
	v_and_or_b32 v73, v73, s1, 7
	v_min3_f32 v213, v211, s4, v214
	v_med3_f32 v211, v212, v70, v71
	v_and_or_b32 v74, v74, s1, 8
	v_min3_f32 v210, v212, v70, v71
	v_mfma_f32_32x32x16_f16 v[82:97], v[122:125], v[202:205], v[82:97]
	v_and_or_b32 v75, v75, s1, 9
	v_med3_f32 v214, v210, v72, v73
	v_and_or_b32 v76, v76, s1, 10
	v_min3_f32 v212, v210, v72, v73
	v_and_or_b32 v77, v77, s1, 11
	v_min3_f32 v213, v213, v211, v214
	v_med3_f32 v211, v212, v74, v75
	v_and_or_b32 v78, v78, s1, 12
	v_mfma_f32_32x32x16_f16 v[82:97], v[126:129], v[206:209], v[82:97]
	v_min3_f32 v210, v212, v74, v75
	v_and_or_b32 v79, v79, s1, 13
	v_med3_f32 v214, v210, v76, v77
	v_and_or_b32 v80, v80, s1, 14
	v_min3_f32 v212, v210, v76, v77
	v_and_or_b32 v81, v81, s1, 15
	v_min3_f32 v213, v213, v211, v214
	v_med3_f32 v211, v212, v78, v79
	v_min3_f32 v210, v212, v78, v79
	v_med3_f32 v214, v210, v80, v81
	v_min3_f32 v212, v210, v80, v81
	v_min3_f32 v213, v213, v211, v214
	v_mfma_f32_32x32x16_f16 v[66:81], v[130:133], v[194:197], v[34:49]
	v_and_or_b32 v82, v82, s1, 16
	v_and_or_b32 v83, v83, s1, 17
	v_and_or_b32 v84, v84, s1, 18
	v_and_or_b32 v85, v85, s1, 19
	v_med3_f32 v211, v212, v82, v83
	v_and_or_b32 v86, v86, s1, 20
	v_min3_f32 v210, v212, v82, v83
	v_and_or_b32 v87, v87, s1, 21
	v_mfma_f32_32x32x16_f16 v[66:81], v[134:137], v[198:201], v[66:81]
	v_med3_f32 v214, v210, v84, v85
	v_and_or_b32 v88, v88, s1, 22
	v_min3_f32 v212, v210, v84, v85
	v_and_or_b32 v89, v89, s1, 23
	v_min3_f32 v213, v213, v211, v214
	v_med3_f32 v211, v212, v86, v87
	v_and_or_b32 v90, v90, s1, 24
	v_min3_f32 v210, v212, v86, v87
	v_mfma_f32_32x32x16_f16 v[66:81], v[138:141], v[202:205], v[66:81]
	v_and_or_b32 v91, v91, s1, 25
	v_med3_f32 v214, v210, v88, v89
	v_and_or_b32 v92, v92, s1, 26
	v_min3_f32 v212, v210, v88, v89
	v_and_or_b32 v93, v93, s1, 27
	v_min3_f32 v213, v213, v211, v214
	v_med3_f32 v211, v212, v90, v91
	v_and_or_b32 v94, v94, s1, 28
	v_mfma_f32_32x32x16_f16 v[66:81], v[142:145], v[206:209], v[66:81]
	v_min3_f32 v210, v212, v90, v91
	v_and_or_b32 v95, v95, s1, 29
	v_med3_f32 v214, v210, v92, v93
	v_and_or_b32 v96, v96, s1, 30
	v_min3_f32 v212, v210, v92, v93
	v_and_or_b32 v97, v97, s1, 31
	v_min3_f32 v213, v213, v211, v214
	v_med3_f32 v211, v212, v94, v95
	v_min3_f32 v210, v212, v94, v95
	v_med3_f32 v214, v210, v96, v97
	v_min3_f32 v212, v210, v96, v97
	v_min3_f32 v213, v213, v211, v214
	v_mfma_f32_32x32x16_f16 v[82:97], v[146:149], v[194:197], v[50:65]
	v_and_or_b32 v66, v66, s1, 32
	v_and_or_b32 v67, v67, s1, 33
	v_and_or_b32 v68, v68, s1, 34
	v_and_or_b32 v69, v69, s1, 35
	v_med3_f32 v211, v212, v66, v67
	v_and_or_b32 v70, v70, s1, 36
	v_min3_f32 v210, v212, v66, v67
	v_and_or_b32 v71, v71, s1, 37
	v_mfma_f32_32x32x16_f16 v[82:97], v[150:153], v[198:201], v[82:97]
	v_med3_f32 v214, v210, v68, v69
	v_and_or_b32 v72, v72, s1, 38
	v_min3_f32 v212, v210, v68, v69
	v_and_or_b32 v73, v73, s1, 39
	v_min3_f32 v213, v213, v211, v214
	v_med3_f32 v211, v212, v70, v71
	v_and_or_b32 v74, v74, s1, 40
	v_min3_f32 v210, v212, v70, v71
	v_mfma_f32_32x32x16_f16 v[82:97], v[154:157], v[202:205], v[82:97]
	v_and_or_b32 v75, v75, s1, 41
	v_med3_f32 v214, v210, v72, v73
	v_and_or_b32 v76, v76, s1, 42
	v_min3_f32 v212, v210, v72, v73
	v_and_or_b32 v77, v77, s1, 43
	v_min3_f32 v213, v213, v211, v214
	v_med3_f32 v211, v212, v74, v75
	v_and_or_b32 v78, v78, s1, 44
	v_mfma_f32_32x32x16_f16 v[82:97], v[158:161], v[206:209], v[82:97]
	v_min3_f32 v210, v212, v74, v75
	v_and_or_b32 v79, v79, s1, 45
	v_med3_f32 v214, v210, v76, v77
	v_and_or_b32 v80, v80, s1, 46
	v_min3_f32 v212, v210, v76, v77
	v_and_or_b32 v81, v81, s1, 47
	v_min3_f32 v213, v213, v211, v214
	v_med3_f32 v211, v212, v78, v79
	v_min3_f32 v210, v212, v78, v79
	v_med3_f32 v214, v210, v80, v81
	v_min3_f32 v212, v210, v80, v81
	v_min3_f32 v213, v213, v211, v214
	v_and_or_b32 v82, v82, s1, 48
	v_and_or_b32 v83, v83, s1, 49
	v_and_or_b32 v84, v84, s1, 50
	v_and_or_b32 v85, v85, s1, 51
	v_med3_f32 v211, v212, v82, v83
	v_and_or_b32 v86, v86, s1, 52
	v_min3_f32 v210, v212, v82, v83
	v_and_or_b32 v87, v87, s1, 53
	v_med3_f32 v214, v210, v84, v85
	v_and_or_b32 v88, v88, s1, 54
	v_min3_f32 v212, v210, v84, v85
	v_and_or_b32 v89, v89, s1, 55
	v_min3_f32 v213, v213, v211, v214
	v_med3_f32 v211, v212, v86, v87
	v_and_or_b32 v90, v90, s1, 56
	v_min3_f32 v210, v212, v86, v87
	v_and_or_b32 v91, v91, s1, 57
	v_med3_f32 v214, v210, v88, v89
	v_and_or_b32 v92, v92, s1, 58
	v_min3_f32 v212, v210, v88, v89
	v_and_or_b32 v93, v93, s1, 59
	v_min3_f32 v213, v213, v211, v214
	v_med3_f32 v211, v212, v90, v91
	v_and_or_b32 v94, v94, s1, 60
	v_min3_f32 v210, v212, v90, v91
	v_and_or_b32 v95, v95, s1, 61
	v_med3_f32 v214, v210, v92, v93
	v_and_or_b32 v96, v96, s1, 62
	v_min3_f32 v212, v210, v92, v93
	v_or_b32_e32 v97, 63, v97
	v_min3_f32 v213, v213, v211, v214
	v_med3_f32 v211, v212, v94, v95
	v_min3_f32 v210, v212, v94, v95
	v_med3_f32 v214, v210, v96, v97
	v_min3_f32 v212, v210, v96, v97
	v_min3_f32 v213, v213, v211, v214
	ds_write_b64 v189, v[212:213]
	s_cmp_gt_u32 s5, 13
	s_cbranch_scc1 .Lld_even_noW
	s_and_b32 s6, s0, 2
	s_waitcnt vmcnt(3)
	v_cvt_pk_f16_f32 v67, v176, v177
	v_cvt_pk_f16_f32 v66, v174, v175
	s_lshl_b32 s6, s6, 13
	ds_write_b64 v192, v[66:67] offset:4608
	s_waitcnt vmcnt(2)
	v_cvt_pk_f16_f32 v67, v172, v173
	v_cvt_pk_f16_f32 v66, v170, v171
	s_or_b32 s6, s6, 0x12000
	ds_write_b64 v192, v[66:67] offset:6912
	v_lshl_or_b32 v66, v187, 4, s6
	ds_write_b128 v66, v[174:177]
	v_lshl_or_b32 v66, v188, 4, s6
	ds_write_b128 v66, v[170:173]
	s_min_u32 s6, s5, 11
	v_lshl_add_u32 v66, s6, 13, v191
	v_or_b32_e32 v66, v66, v178
	v_or_b32_e32 v67, 0x1000, v66
	global_load_dwordx4 v[174:177], v66, s[20:21] nt
	global_load_dwordx4 v[170:173], v67, s[20:21] nt
	s_waitcnt lgkmcnt(4)
	s_barrier
.Lld_odd:
	ds_read_b128 v[194:197], v193 offset:4608
	ds_read_b128 v[198:201], v193 offset:4640
	ds_read_b128 v[202:205], v193 offset:4672
	ds_read_b128 v[206:209], v193 offset:4704
	s_add_i32 s0, s0, 2
	v_add_u32_e32 v192, 0x2400, v192
	v_add_u32_e32 v193, 0x2400, v193
	s_waitcnt lgkmcnt(3)
	v_mfma_f32_32x32x16_f16 v[66:81], v[98:101], v[194:197], v[2:17]
	s_waitcnt lgkmcnt(2)
	v_mfma_f32_32x32x16_f16 v[66:81], v[102:105], v[198:201], v[66:81]
	s_waitcnt lgkmcnt(1)
	v_mfma_f32_32x32x16_f16 v[66:81], v[106:109], v[202:205], v[66:81]
	s_waitcnt lgkmcnt(0)
	v_mfma_f32_32x32x16_f16 v[66:81], v[110:113], v[206:209], v[66:81]
	v_mfma_f32_32x32x16_f16 v[82:97], v[114:117], v[194:197], v[18:33]
	s_nop 10
	v_and_b32_e32 v66, 0xffffffc0, v66
	v_and_or_b32 v67, v67, s1, 1
	v_and_or_b32 v68, v68, s1, 2
	v_and_or_b32 v69, v69, s1, 3
	v_med3_f32 v211, v66, v67, s4
	v_and_or_b32 v70, v70, s1, 4
	v_min3_f32 v210, v66, s4, v67
	v_and_or_b32 v71, v71, s1, 5
	v_mfma_f32_32x32x16_f16 v[82:97], v[118:121], v[198:201], v[82:97]
	v_med3_f32 v214, v210, v68, v69
	v_and_or_b32 v72, v72, s1, 6
	v_min3_f32 v212, v210, v68, v69
	v_and_or_b32 v73, v73, s1, 7
	v_min3_f32 v213, v211, s4, v214
	v_med3_f32 v211, v212, v70, v71
	v_and_or_b32 v74, v74, s1, 8
	v_min3_f32 v210, v212, v70, v71
	v_mfma_f32_32x32x16_f16 v[82:97], v[122:125], v[202:205], v[82:97]
	v_and_or_b32 v75, v75, s1, 9
	v_med3_f32 v214, v210, v72, v73
	v_and_or_b32 v76, v76, s1, 10
	v_min3_f32 v212, v210, v72, v73
	v_and_or_b32 v77, v77, s1, 11
	v_min3_f32 v213, v213, v211, v214
	v_med3_f32 v211, v212, v74, v75
	v_and_or_b32 v78, v78, s1, 12
	v_mfma_f32_32x32x16_f16 v[82:97], v[126:129], v[206:209], v[82:97]
	v_min3_f32 v210, v212, v74, v75
	v_and_or_b32 v79, v79, s1, 13
	v_med3_f32 v214, v210, v76, v77
	v_and_or_b32 v80, v80, s1, 14
	v_min3_f32 v212, v210, v76, v77
	v_and_or_b32 v81, v81, s1, 15
	v_min3_f32 v213, v213, v211, v214
	v_med3_f32 v211, v212, v78, v79
	v_min3_f32 v210, v212, v78, v79
	v_med3_f32 v214, v210, v80, v81
	v_min3_f32 v212, v210, v80, v81
	v_min3_f32 v213, v213, v211, v214
	v_mfma_f32_32x32x16_f16 v[66:81], v[130:133], v[194:197], v[34:49]
	v_and_or_b32 v82, v82, s1, 16
	v_and_or_b32 v83, v83, s1, 17
	v_and_or_b32 v84, v84, s1, 18
	v_and_or_b32 v85, v85, s1, 19
	v_med3_f32 v211, v212, v82, v83
	v_and_or_b32 v86, v86, s1, 20
	v_min3_f32 v210, v212, v82, v83
	v_and_or_b32 v87, v87, s1, 21
	v_mfma_f32_32x32x16_f16 v[66:81], v[134:137], v[198:201], v[66:81]
	v_med3_f32 v214, v210, v84, v85
	v_and_or_b32 v88, v88, s1, 22
	v_min3_f32 v212, v210, v84, v85
	v_and_or_b32 v89, v89, s1, 23
	v_min3_f32 v213, v213, v211, v214
	v_med3_f32 v211, v212, v86, v87
	v_and_or_b32 v90, v90, s1, 24
	v_min3_f32 v210, v212, v86, v87
	v_mfma_f32_32x32x16_f16 v[66:81], v[138:141], v[202:205], v[66:81]
	v_and_or_b32 v91, v91, s1, 25
	v_med3_f32 v214, v210, v88, v89
	v_and_or_b32 v92, v92, s1, 26
	v_min3_f32 v212, v210, v88, v89
	v_and_or_b32 v93, v93, s1, 27
	v_min3_f32 v213, v213, v211, v214
	v_med3_f32 v211, v212, v90, v91
	v_and_or_b32 v94, v94, s1, 28
	v_mfma_f32_32x32x16_f16 v[66:81], v[142:145], v[206:209], v[66:81]
	v_min3_f32 v210, v212, v90, v91
	v_and_or_b32 v95, v95, s1, 29
	v_med3_f32 v214, v210, v92, v93
	v_and_or_b32 v96, v96, s1, 30
	v_min3_f32 v212, v210, v92, v93
	v_and_or_b32 v97, v97, s1, 31
	v_min3_f32 v213, v213, v211, v214
	v_med3_f32 v211, v212, v94, v95
	v_min3_f32 v210, v212, v94, v95
	v_med3_f32 v214, v210, v96, v97
	v_min3_f32 v212, v210, v96, v97
	v_min3_f32 v213, v213, v211, v214
	v_mfma_f32_32x32x16_f16 v[82:97], v[146:149], v[194:197], v[50:65]
	v_and_or_b32 v66, v66, s1, 32
	v_and_or_b32 v67, v67, s1, 33
	v_and_or_b32 v68, v68, s1, 34
	v_and_or_b32 v69, v69, s1, 35
	v_med3_f32 v211, v212, v66, v67
	v_and_or_b32 v70, v70, s1, 36
	v_min3_f32 v210, v212, v66, v67
	v_and_or_b32 v71, v71, s1, 37
	v_mfma_f32_32x32x16_f16 v[82:97], v[150:153], v[198:201], v[82:97]
	v_med3_f32 v214, v210, v68, v69
	v_and_or_b32 v72, v72, s1, 38
	v_min3_f32 v212, v210, v68, v69
	v_and_or_b32 v73, v73, s1, 39
	v_min3_f32 v213, v213, v211, v214
	v_med3_f32 v211, v212, v70, v71
	v_and_or_b32 v74, v74, s1, 40
	v_min3_f32 v210, v212, v70, v71
	v_mfma_f32_32x32x16_f16 v[82:97], v[154:157], v[202:205], v[82:97]
	v_and_or_b32 v75, v75, s1, 41
	v_med3_f32 v214, v210, v72, v73
	v_and_or_b32 v76, v76, s1, 42
	v_min3_f32 v212, v210, v72, v73
	v_and_or_b32 v77, v77, s1, 43
	v_min3_f32 v213, v213, v211, v214
	v_med3_f32 v211, v212, v74, v75
	v_and_or_b32 v78, v78, s1, 44
	v_mfma_f32_32x32x16_f16 v[82:97], v[158:161], v[206:209], v[82:97]
	v_min3_f32 v210, v212, v74, v75
	v_and_or_b32 v79, v79, s1, 45
	v_med3_f32 v214, v210, v76, v77
	v_and_or_b32 v80, v80, s1, 46
	v_min3_f32 v212, v210, v76, v77
	v_and_or_b32 v81, v81, s1, 47
	v_min3_f32 v213, v213, v211, v214
	v_med3_f32 v211, v212, v78, v79
	v_min3_f32 v210, v212, v78, v79
	v_med3_f32 v214, v210, v80, v81
	v_min3_f32 v212, v210, v80, v81
	v_min3_f32 v213, v213, v211, v214
	v_and_or_b32 v82, v82, s1, 48
	v_and_or_b32 v83, v83, s1, 49
	v_and_or_b32 v84, v84, s1, 50
	v_and_or_b32 v85, v85, s1, 51
	v_med3_f32 v211, v212, v82, v83
	v_and_or_b32 v86, v86, s1, 52
	v_min3_f32 v210, v212, v82, v83
	v_and_or_b32 v87, v87, s1, 53
	v_med3_f32 v214, v210, v84, v85
	v_and_or_b32 v88, v88, s1, 54
	v_min3_f32 v212, v210, v84, v85
	v_and_or_b32 v89, v89, s1, 55
	v_min3_f32 v213, v213, v211, v214
	v_med3_f32 v211, v212, v86, v87
	v_and_or_b32 v90, v90, s1, 56
	v_min3_f32 v210, v212, v86, v87
	v_and_or_b32 v91, v91, s1, 57
	v_med3_f32 v214, v210, v88, v89
	v_and_or_b32 v92, v92, s1, 58
	v_min3_f32 v212, v210, v88, v89
	v_and_or_b32 v93, v93, s1, 59
	v_min3_f32 v213, v213, v211, v214
	v_med3_f32 v211, v212, v90, v91
	v_and_or_b32 v94, v94, s1, 60
	v_min3_f32 v210, v212, v90, v91
	v_and_or_b32 v95, v95, s1, 61
	v_med3_f32 v214, v210, v92, v93
	v_and_or_b32 v96, v96, s1, 62
	v_min3_f32 v212, v210, v92, v93
	v_or_b32_e32 v97, 63, v97
	v_min3_f32 v213, v213, v211, v214
	v_med3_f32 v211, v212, v94, v95
	v_min3_f32 v210, v212, v94, v95
	v_med3_f32 v214, v210, v96, v97
	v_min3_f32 v212, v210, v96, v97
	v_min3_f32 v213, v213, v211, v214
	ds_write_b64 v189, v[212:213] offset:4608
	s_cmp_gt_u32 s5, 13
	s_cbranch_scc1 .Lld_exit
	s_waitcnt vmcnt(3)
	v_cvt_pk_f16_f32 v67, v168, v169
	v_cvt_pk_f16_f32 v66, v166, v167
	ds_write_b64 v192, v[66:67]
	s_waitcnt vmcnt(2)
	v_cvt_pk_f16_f32 v67, v164, v165
	v_cvt_pk_f16_f32 v66, v162, v163
	ds_write_b64 v192, v[66:67] offset:2304
	s_add_i32 s6, s0, -1
	s_add_i32 s5, s0, -2
	s_and_b32 s6, s6, 3
	s_min_u32 s7, s5, 12
	s_lshl_b32 s6, s6, 13
	v_lshl_add_u32 v66, s7, 13, v190
	s_add_i32 s6, s6, 0x12000
	v_or_b32_e32 v66, v66, v178
	v_lshl_or_b32 v67, v187, 4, s6
	v_lshl_or_b32 v84, v188, 4, s6
	v_or_b32_e32 v85, 0x1000, v66
	ds_write_b128 v67, v[166:169]
	ds_write_b128 v84, v[162:165]
	global_load_dwordx4 v[166:169], v66, s[20:21] nt
	global_load_dwordx4 v[162:165], v85, s[20:21] nt
	s_waitcnt lgkmcnt(4)
	s_barrier
	s_branch .Lld_even
.Lld_even_noW:
	s_waitcnt lgkmcnt(0)
	s_barrier
	s_branch .Lld_odd

.LBB0_85:
	s_waitcnt vmcnt(3)
	v_mov_b32_e32 v167, 0
	s_and_b64 vcc, exec, s[0:1]
	s_cbranch_vccz .LBB0_107
	s_lshl_b32 s0, s33, 2
	s_and_b32 s0, s0, 12
	v_bfe_u32 v192, v0, 3, 2
	s_waitcnt vmcnt(0)
	v_or3_b32 v172, v192, s0, v182
	v_and_b32_e32 v170, 7, v0
	s_setprio 2
	v_mov_b32_e32 v222, 0
	v_mov_b32_e32 v223, 0
	ds_read_b128 v[162:165], v179
	ds_read_b128 v[166:169], v179 offset:32
	ds_read_b128 v[174:177], v179 offset:64
	ds_read_b128 v[188:191], v179 offset:96
	s_movk_i32 s16, 0xffc0
	s_mov_b32 s25, 0x7f61b1e6
	s_waitcnt lgkmcnt(0)
	v_mfma_f32_32x32x16_f16 v[66:81], v[98:101], v[162:165], v[2:17]
	s_lshl_b32 s1, s33, 4
	s_add_i32 s1, s1, 0x1a000
	s_mov_b32 s4, 0x1a000
	v_cmp_eq_u32_e32 vcc, 0, v170
	s_mov_b32 s17, 1
	v_add_u32_e32 v179, 0x1200, v179
	s_mov_b32 s26, 0x3d3851ec
	v_mfma_f32_32x32x16_f16 v[66:81], v[102:105], v[166:169], v[66:81]
	s_movk_i32 s27, 0x3ff
	s_movk_i32 s28, 0x3ff0
	v_mfma_f32_32x32x16_f16 v[66:81], v[106:109], v[174:177], v[66:81]
	v_mfma_f32_32x32x16_f16 v[66:81], v[110:113], v[188:191], v[66:81]
	s_nop 11
	v_and_b32_e32 v82, 0xffffffc0, v66
	v_and_or_b32 v83, v67, s16, 1
	v_and_or_b32 v84, v68, s16, 2
	v_and_or_b32 v85, v69, s16, 3
	v_and_or_b32 v86, v70, s16, 4
	v_and_or_b32 v87, v71, s16, 5
	v_and_or_b32 v88, v72, s16, 6
	v_and_or_b32 v89, v73, s16, 7
	v_and_or_b32 v90, v74, s16, 8
	v_and_or_b32 v91, v75, s16, 9
	v_and_or_b32 v92, v76, s16, 10
	v_and_or_b32 v93, v77, s16, 11
	v_and_or_b32 v94, v78, s16, 12
	v_and_or_b32 v95, v79, s16, 13
	v_and_or_b32 v96, v80, s16, 14
	v_and_or_b32 v97, v81, s16, 15
	v_mfma_f32_32x32x16_f16 v[66:81], v[114:117], v[162:165], v[18:33]
	v_med3_f32 v171, v82, v83, s25
	v_min3_f32 v82, v82, s25, v83
	v_med3_f32 v83, v82, v84, v85
	v_min3_f32 v82, v82, v84, v85
	v_med3_f32 v84, v82, v86, v87
	v_min3_f32 v82, v82, v86, v87
	v_min3_f32 v83, v171, s25, v83
	v_mfma_f32_32x32x16_f16 v[66:81], v[118:121], v[166:169], v[66:81]
	v_med3_f32 v85, v82, v88, v89
	v_min3_f32 v82, v82, v88, v89
	v_min3_f32 v83, v83, v84, v85
	v_med3_f32 v84, v82, v90, v91
	v_min3_f32 v82, v82, v90, v91
	v_med3_f32 v85, v82, v92, v93
	v_min3_f32 v82, v82, v92, v93
	v_mfma_f32_32x32x16_f16 v[66:81], v[122:125], v[174:177], v[66:81]
	v_min3_f32 v83, v83, v84, v85
	v_med3_f32 v84, v82, v94, v95
	v_min3_f32 v82, v82, v94, v95
	v_med3_f32 v85, v82, v96, v97
	v_min3_f32 v171, v82, v96, v97
	v_min3_f32 v173, v83, v84, v85
	v_mfma_f32_32x32x16_f16 v[66:81], v[126:129], v[188:191], v[66:81]
	v_mfma_f32_32x32x16_f16 v[82:97], v[130:133], v[162:165], v[34:49]
	s_nop 10
	v_and_or_b32 v66, v66, s16, 16
	v_and_or_b32 v67, v67, s16, 17
	v_and_or_b32 v68, v68, s16, 18
	v_and_or_b32 v69, v69, s16, 19
	v_med3_f32 v187, v171, v66, v67
	v_min3_f32 v66, v171, v66, v67
	v_and_or_b32 v70, v70, s16, 20
	v_and_or_b32 v71, v71, s16, 21
	v_med3_f32 v67, v66, v68, v69
	v_min3_f32 v66, v66, v68, v69
	v_and_or_b32 v72, v72, s16, 22
	v_and_or_b32 v73, v73, s16, 23
	v_med3_f32 v68, v66, v70, v71
	v_min3_f32 v66, v66, v70, v71
	v_and_or_b32 v74, v74, s16, 24
	v_and_or_b32 v75, v75, s16, 25
	v_min3_f32 v67, v173, v187, v67
	v_med3_f32 v69, v66, v72, v73
	v_min3_f32 v66, v66, v72, v73
	v_and_or_b32 v76, v76, s16, 26
	v_and_or_b32 v77, v77, s16, 27
	v_min3_f32 v67, v67, v68, v69
	v_med3_f32 v68, v66, v74, v75
	v_min3_f32 v66, v66, v74, v75
	v_and_or_b32 v78, v78, s16, 28
	v_and_or_b32 v79, v79, s16, 29
	v_med3_f32 v69, v66, v76, v77
	v_min3_f32 v66, v66, v76, v77
	v_and_or_b32 v80, v80, s16, 30
	v_and_or_b32 v81, v81, s16, 31
	v_min3_f32 v67, v67, v68, v69
	v_med3_f32 v68, v66, v78, v79
	v_min3_f32 v66, v66, v78, v79
	v_med3_f32 v69, v66, v80, v81
	v_mfma_f32_32x32x16_f16 v[82:97], v[134:137], v[166:169], v[82:97]
	v_min3_f32 v171, v66, v80, v81
	v_min3_f32 v173, v67, v68, v69
	v_mfma_f32_32x32x16_f16 v[66:81], v[146:149], v[162:165], v[50:65]
	v_mfma_f32_32x32x16_f16 v[82:97], v[138:141], v[174:177], v[82:97]
	v_mfma_f32_32x32x16_f16 v[66:81], v[150:153], v[166:169], v[66:81]
	v_mov_b32_e32 v167, 0
	v_mfma_f32_32x32x16_f16 v[82:97], v[142:145], v[188:191], v[82:97]
	v_mfma_f32_32x32x16_f16 v[66:81], v[154:157], v[174:177], v[66:81]
	s_nop 10
	v_and_or_b32 v82, v82, s16, 32
	v_and_or_b32 v83, v83, s16, 33
	v_and_or_b32 v84, v84, s16, 34
	v_and_or_b32 v85, v85, s16, 35
	v_med3_f32 v162, v171, v82, v83
	v_min3_f32 v82, v171, v82, v83
	v_and_or_b32 v86, v86, s16, 36
	v_mfma_f32_32x32x16_f16 v[66:81], v[158:161], v[188:191], v[66:81]
	v_and_or_b32 v87, v87, s16, 37
	v_med3_f32 v83, v82, v84, v85
	v_min3_f32 v82, v82, v84, v85
	v_and_or_b32 v88, v88, s16, 38
	v_and_or_b32 v89, v89, s16, 39
	v_med3_f32 v84, v82, v86, v87
	v_min3_f32 v82, v82, v86, v87
	v_and_or_b32 v90, v90, s16, 40
	v_and_or_b32 v91, v91, s16, 41
	v_min3_f32 v83, v173, v162, v83
	v_med3_f32 v85, v82, v88, v89
	v_min3_f32 v82, v82, v88, v89
	v_and_or_b32 v92, v92, s16, 42
	v_and_or_b32 v93, v93, s16, 43
	v_min3_f32 v83, v83, v84, v85
	v_med3_f32 v84, v82, v90, v91
	v_min3_f32 v82, v82, v90, v91
	v_and_or_b32 v94, v94, s16, 44
	v_and_or_b32 v95, v95, s16, 45
	v_med3_f32 v85, v82, v92, v93
	v_min3_f32 v82, v82, v92, v93
	v_and_or_b32 v96, v96, s16, 46
	v_and_or_b32 v97, v97, s16, 47
	v_min3_f32 v83, v83, v84, v85
	v_med3_f32 v84, v82, v94, v95
	v_min3_f32 v82, v82, v94, v95
	v_med3_f32 v85, v82, v96, v97
	v_min3_f32 v82, v82, v96, v97
	v_and_or_b32 v66, v66, s16, 48
	v_and_or_b32 v67, v67, s16, 49
	v_min3_f32 v83, v83, v84, v85
	v_and_or_b32 v68, v68, s16, 50
	v_and_or_b32 v69, v69, s16, 51
	v_med3_f32 v84, v82, v66, v67
	v_min3_f32 v66, v82, v66, v67
	v_and_or_b32 v70, v70, s16, 52
	v_and_or_b32 v71, v71, s16, 53
	v_med3_f32 v67, v66, v68, v69
	v_min3_f32 v66, v66, v68, v69
	v_and_or_b32 v72, v72, s16, 54
	v_and_or_b32 v73, v73, s16, 55
	v_med3_f32 v68, v66, v70, v71
	v_min3_f32 v66, v66, v70, v71
	v_and_or_b32 v74, v74, s16, 56
	v_and_or_b32 v75, v75, s16, 57
	v_min3_f32 v67, v83, v84, v67
	v_med3_f32 v69, v66, v72, v73
	v_min3_f32 v66, v66, v72, v73
	v_and_or_b32 v76, v76, s16, 58
	v_and_or_b32 v77, v77, s16, 59
	v_min3_f32 v67, v67, v68, v69
	v_med3_f32 v68, v66, v74, v75
	v_min3_f32 v66, v66, v74, v75
	v_and_or_b32 v78, v78, s16, 60
	v_and_or_b32 v79, v79, s16, 61
	v_med3_f32 v69, v66, v76, v77
	v_min3_f32 v66, v66, v76, v77
	v_and_or_b32 v80, v80, s16, 62
	v_or_b32_e32 v81, 63, v81
	v_min3_f32 v67, v67, v68, v69
	v_med3_f32 v68, v66, v78, v79
	v_min3_f32 v66, v66, v78, v79
	v_med3_f32 v69, v66, v80, v81
	v_min3_f32 v67, v67, v68, v69
	v_lshlrev_b32_e32 v68, 3, v184
	v_min3_f32 v66, v66, v80, v81
	v_add3_u32 v177, s1, v185, v68
	ds_write_b64 v177, v[66:67]
	v_mul_u32_u24_e32 v66, 0x90, v172
	v_lshlrev_b32_e32 v67, 4, v170
	v_add3_u32 v185, v67, v66, s4
	v_and_b32_e32 v66, 0xff, v0
	v_mov_b32_e32 v67, 0x12000
	v_or_b32_e32 v173, 16, v183
	s_mov_b32 s1, 0x12000
	v_lshl_or_b32 v175, v66, 4, v67
	v_lshlrev_b32_e32 v66, 8, v173
	v_or3_b32 v174, v66, v178, s1
	s_lshl_b32 s1, s2, 17
	v_or3_b32 v166, s1, v186, v178
	s_waitcnt lgkmcnt(0)
	s_barrier
	v_lshl_add_u64 v[168:169], s[12:13], 0, v[166:167]
	v_or_b32_e32 v166, 0x1000, v166
	v_lshlrev_b32_e32 v176, 7, v170
	v_lshl_add_u64 v[170:171], s[12:13], 0, v[166:167]
	v_add3_u32 v166, v182, s0, v192
	v_mov_b32_e32 v66, 0x20c00
	v_or_b32_e32 v187, 4, v176
	v_lshlrev_b32_e32 v188, 2, v183
	v_lshl_or_b32 v186, v166, 2, v66
	v_mov_b32_e32 v189, 0x21d44
	s_mov_b64 s[4:5], 0x2000
	v_bfrev_b32_e32 v190, 1
.LBB0_88:
	s_add_i32 s29, s17, -1
	s_and_b32 s0, s29, 1
	s_mulk_i32 s0, 0x1200
	v_add_u32_e32 v254, s0, v185
	ds_read_b128 v[250:253], v254
	ds_read_b128 v[194:197], v179
	ds_read_b128 v[198:201], v179 offset:32
	ds_read_b128 v[202:205], v179 offset:64
	ds_read_b128 v[206:209], v179 offset:96
	s_cmp_lt_u32 s17, 2
	s_cbranch_scc1 .Low_noout
	v_cmp_lt_i32_e64 s[0:1], -1, v192
	s_waitcnt vmcnt(0)
	s_and_saveexec_b64 s[6:7], s[0:1]
	s_cbranch_execz .Low_a_donel
	v_pk_add_f32 v[66:67], v[246:247], v[224:225] neg_lo:[0,1] neg_hi:[0,1]
	v_pk_add_f32 v[74:75], v[248:249], v[226:227] neg_lo:[0,1] neg_hi:[0,1]
	v_pk_fma_f32 v[222:223], v[66:67], v[66:67], v[222:223]
	v_pk_fma_f32 v[222:223], v[74:75], v[74:75], v[222:223]
	v_pk_add_f32 v[66:67], v[224:225], v[66:67]
	v_pk_add_f32 v[68:69], v[226:227], v[74:75]
	global_store_dwordx4 v[168:169], v[66:69], off sc0 sc1
	s_nop 1

.Low_m_done:
	s_or_b64 exec, exec, s[6:7]
	s_waitcnt lgkmcnt(1)
	v_mfma_f32_32x32x16_f16 v[66:81], v[98:101], v[194:197], v[2:17]
	v_mfma_f32_32x32x16_f16 v[66:81], v[102:105], v[198:201], v[66:81]
	v_add_u32_e32 v254, 0x20c00, v188
	s_waitcnt lgkmcnt(0)
	ds_read_b32 v191, v254 offset:64
	ds_read_b32 v192, v254
	v_mfma_f32_32x32x16_f16 v[66:81], v[106:109], v[202:205], v[66:81]
	v_mfma_f32_32x32x16_f16 v[66:81], v[110:113], v[206:209], v[66:81]
	v_mfma_f32_32x32x16_f16 v[82:97], v[114:117], v[194:197], v[18:33]
	s_waitcnt lgkmcnt(0)
	v_and_b32_e32 v212, s27, v191
	v_lshl_or_b32 v212, v212, 8, v178
	global_load_dwordx4 v[162:165], v212, s[22:23]
	v_and_b32_e32 v213, s27, v192
	v_lshl_or_b32 v213, v213, 8, v178
	global_load_dwordx4 v[246:249], v213, s[22:23]
	s_and_b32 s1, s29, 3
	v_lshl_add_u32 v212, s1, 13, v175
	v_lshl_add_u32 v213, s1, 13, v174
	ds_read_b128 v[224:227], v212
	ds_read_b128 v[228:231], v213
	v_and_b32_e32 v66, 0xffffffc0, v66
	v_and_or_b32 v67, v67, s16, 1
	v_and_or_b32 v68, v68, s16, 2
	v_and_or_b32 v69, v69, s16, 3
	v_med3_f32 v211, v66, v67, s25
	v_and_or_b32 v70, v70, s16, 4
	v_min3_f32 v210, v66, s25, v67
	v_and_or_b32 v71, v71, s16, 5
	v_mfma_f32_32x32x16_f16 v[82:97], v[118:121], v[198:201], v[82:97]
	v_med3_f32 v214, v210, v68, v69
	v_and_or_b32 v72, v72, s16, 6
	v_min3_f32 v212, v210, v68, v69
	v_and_or_b32 v73, v73, s16, 7
	v_min3_f32 v213, v211, s25, v214
	v_med3_f32 v211, v212, v70, v71
	v_and_or_b32 v74, v74, s16, 8
	v_min3_f32 v210, v212, v70, v71
	v_mfma_f32_32x32x16_f16 v[82:97], v[122:125], v[202:205], v[82:97]
	v_and_or_b32 v75, v75, s16, 9
	v_med3_f32 v214, v210, v72, v73
	v_and_or_b32 v76, v76, s16, 10
	v_min3_f32 v212, v210, v72, v73
	v_and_or_b32 v77, v77, s16, 11
	v_min3_f32 v213, v213, v211, v214
	v_med3_f32 v211, v212, v74, v75
	v_and_or_b32 v78, v78, s16, 12
	v_mfma_f32_32x32x16_f16 v[82:97], v[126:129], v[206:209], v[82:97]
	v_min3_f32 v210, v212, v74, v75
	v_and_or_b32 v79, v79, s16, 13
	v_med3_f32 v214, v210, v76, v77
	v_and_or_b32 v80, v80, s16, 14
	v_min3_f32 v212, v210, v76, v77
	v_and_or_b32 v81, v81, s16, 15
	v_min3_f32 v213, v213, v211, v214
	v_med3_f32 v211, v212, v78, v79
	v_min3_f32 v210, v212, v78, v79
	v_med3_f32 v214, v210, v80, v81
	v_min3_f32 v212, v210, v80, v81
	v_min3_f32 v213, v213, v211, v214
	v_mfma_f32_32x32x16_f16 v[66:81], v[130:133], v[194:197], v[34:49]
	v_and_or_b32 v82, v82, s16, 16
	v_and_or_b32 v83, v83, s16, 17
	v_and_or_b32 v84, v84, s16, 18
	v_and_or_b32 v85, v85, s16, 19
	v_med3_f32 v211, v212, v82, v83
	v_and_or_b32 v86, v86, s16, 20
	v_min3_f32 v210, v212, v82, v83
	v_and_or_b32 v87, v87, s16, 21
	v_mfma_f32_32x32x16_f16 v[66:81], v[134:137], v[198:201], v[66:81]
	v_med3_f32 v214, v210, v84, v85
	v_and_or_b32 v88, v88, s16, 22
	v_min3_f32 v212, v210, v84, v85
	v_and_or_b32 v89, v89, s16, 23
	v_min3_f32 v213, v213, v211, v214
	v_med3_f32 v211, v212, v86, v87
	v_and_or_b32 v90, v90, s16, 24
	v_min3_f32 v210, v212, v86, v87
	v_mfma_f32_32x32x16_f16 v[66:81], v[138:141], v[202:205], v[66:81]
	v_and_or_b32 v91, v91, s16, 25
	v_med3_f32 v214, v210, v88, v89
	v_and_or_b32 v92, v92, s16, 26
	v_min3_f32 v212, v210, v88, v89
	v_and_or_b32 v93, v93, s16, 27
	v_min3_f32 v213, v213, v211, v214
	v_med3_f32 v211, v212, v90, v91
	v_and_or_b32 v94, v94, s16, 28
	v_mfma_f32_32x32x16_f16 v[66:81], v[142:145], v[206:209], v[66:81]
	v_min3_f32 v210, v212, v90, v91
	v_and_or_b32 v95, v95, s16, 29
	v_med3_f32 v214, v210, v92, v93
	v_and_or_b32 v96, v96, s16, 30
	v_min3_f32 v212, v210, v92, v93
	v_and_or_b32 v97, v97, s16, 31
	v_min3_f32 v213, v213, v211, v214
	v_med3_f32 v211, v212, v94, v95
	v_min3_f32 v210, v212, v94, v95
	v_med3_f32 v214, v210, v96, v97
	v_min3_f32 v212, v210, v96, v97
	v_min3_f32 v213, v213, v211, v214
	v_mfma_f32_32x32x16_f16 v[82:97], v[146:149], v[194:197], v[50:65]
	v_and_or_b32 v66, v66, s16, 32
	v_and_or_b32 v67, v67, s16, 33
	v_and_or_b32 v68, v68, s16, 34
	v_and_or_b32 v69, v69, s16, 35
	v_med3_f32 v211, v212, v66, v67
	v_and_or_b32 v70, v70, s16, 36
	v_min3_f32 v210, v212, v66, v67
	v_and_or_b32 v71, v71, s16, 37
	v_mfma_f32_32x32x16_f16 v[82:97], v[150:153], v[198:201], v[82:97]
	v_med3_f32 v214, v210, v68, v69
	v_and_or_b32 v72, v72, s16, 38
	v_min3_f32 v212, v210, v68, v69
	v_and_or_b32 v73, v73, s16, 39
	v_min3_f32 v213, v213, v211, v214
	v_med3_f32 v211, v212, v70, v71
	v_and_or_b32 v74, v74, s16, 40
	v_min3_f32 v210, v212, v70, v71
	v_mfma_f32_32x32x16_f16 v[82:97], v[154:157], v[202:205], v[82:97]
	v_and_or_b32 v75, v75, s16, 41
	v_med3_f32 v214, v210, v72, v73
	v_and_or_b32 v76, v76, s16, 42
	v_min3_f32 v212, v210, v72, v73
	v_and_or_b32 v77, v77, s16, 43
	v_min3_f32 v213, v213, v211, v214
	v_med3_f32 v211, v212, v74, v75
	v_and_or_b32 v78, v78, s16, 44
	v_mfma_f32_32x32x16_f16 v[82:97], v[158:161], v[206:209], v[82:97]
	v_min3_f32 v210, v212, v74, v75
	v_and_or_b32 v79, v79, s16, 45
	v_med3_f32 v214, v210, v76, v77
	v_and_or_b32 v80, v80, s16, 46
	v_min3_f32 v212, v210, v76, v77
	v_and_or_b32 v81, v81, s16, 47
	v_min3_f32 v213, v213, v211, v214
	v_med3_f32 v211, v212, v78, v79
	v_min3_f32 v210, v212, v78, v79
	v_med3_f32 v214, v210, v80, v81
	v_min3_f32 v212, v210, v80, v81
	v_min3_f32 v213, v213, v211, v214
	v_and_or_b32 v82, v82, s16, 48
	v_and_or_b32 v83, v83, s16, 49
	v_and_or_b32 v84, v84, s16, 50
	v_and_or_b32 v85, v85, s16, 51
	v_med3_f32 v211, v212, v82, v83
	v_and_or_b32 v86, v86, s16, 52
	v_min3_f32 v210, v212, v82, v83
	v_and_or_b32 v87, v87, s16, 53
	v_med3_f32 v214, v210, v84, v85
	v_and_or_b32 v88, v88, s16, 54
	v_min3_f32 v212, v210, v84, v85
	v_and_or_b32 v89, v89, s16, 55
	v_min3_f32 v213, v213, v211, v214
	v_med3_f32 v211, v212, v86, v87
	v_and_or_b32 v90, v90, s16, 56
	v_min3_f32 v210, v212, v86, v87
	v_and_or_b32 v91, v91, s16, 57
	v_med3_f32 v214, v210, v88, v89
	v_and_or_b32 v92, v92, s16, 58
	v_min3_f32 v212, v210, v88, v89
	v_and_or_b32 v93, v93, s16, 59
	v_min3_f32 v213, v213, v211, v214
	v_med3_f32 v211, v212, v90, v91
	v_and_or_b32 v94, v94, s16, 60
	v_min3_f32 v210, v212, v90, v91
	v_and_or_b32 v95, v95, s16, 61
	v_med3_f32 v214, v210, v92, v93
	v_and_or_b32 v96, v96, s16, 62
	v_min3_f32 v212, v210, v92, v93
	v_or_b32_e32 v97, 63, v97
	v_min3_f32 v213, v213, v211, v214
	v_med3_f32 v211, v212, v94, v95
	v_min3_f32 v210, v212, v94, v95
	v_med3_f32 v214, v210, v96, v97
	v_min3_f32 v212, v210, v96, v97
	v_min3_f32 v213, v213, v211, v214
	s_and_b32 s0, s17, 1
	s_mulk_i32 s0, 0x1200
	v_add_u32_e32 v254, s0, v177
	ds_write_b64 v254, v[212:213]
	v_add_u32_e32 v179, 0x1200, v179
	v_add_u32_e32 v188, 0x80, v188
	v_add_u32_e32 v186, 0x80, v186
	v_add_u32_e32 v166, 32, v166
	s_add_i32 s17, s17, 1
	s_cmp_lg_u32 s17, 16
	s_waitcnt lgkmcnt(0)
	s_barrier
	s_cbranch_scc1 .LBB0_88
